# ffn_up_row_index_prefetch_no_immediate_wait
# speedup vs baseline: 1.0229x; 1.0013x over previous
.LBB0_959:
	s_add_u32 s20, s20, s24
	s_addc_u32 s21, s21, s25
	s_mov_b32 s19, 8
	s_cmp_lt_i32 s19, 1
	s_cbranch_scc1 .LBB0_965
	s_and_b64 s[24:25], exec, s[4:5]
	v_mov_b32_e32 v34, 0
	s_cselect_b32 s25, s21, s7
	s_cselect_b32 s24, s20, s6
	s_mov_b32 s60, 2
	s_mov_b64 s[26:27], 0x80
	v_mov_b32_e32 v35, v34
	v_mov_b32_e32 v36, v34
	v_mov_b32_e32 v37, v34
	v_mov_b32_e32 v38, v34
	v_mov_b32_e32 v39, v34
	v_mov_b32_e32 v40, v34
	v_mov_b32_e32 v41, v34
	v_mov_b32_e32 v50, v34
	v_mov_b32_e32 v51, v34
	v_mov_b32_e32 v52, v34
	v_mov_b32_e32 v53, v34
	v_mov_b32_e32 v54, v34
	v_mov_b32_e32 v55, v34
	v_mov_b32_e32 v56, v34
	v_mov_b32_e32 v57, v34
	v_mov_b32_e32 v66, v34
	v_mov_b32_e32 v67, v34
	v_mov_b32_e32 v68, v34
	v_mov_b32_e32 v69, v34
	v_mov_b32_e32 v70, v34
	v_mov_b32_e32 v71, v34
	v_mov_b32_e32 v72, v34
	v_mov_b32_e32 v73, v34
	v_mov_b32_e32 v82, v34
	v_mov_b32_e32 v83, v34
	v_mov_b32_e32 v84, v34
	v_mov_b32_e32 v85, v34
	v_mov_b32_e32 v86, v34
	v_mov_b32_e32 v87, v34
	v_mov_b32_e32 v88, v34
	v_mov_b32_e32 v89, v34
	v_mov_b32_e32 v42, v34
	v_mov_b32_e32 v43, v34
	v_mov_b32_e32 v44, v34
	v_mov_b32_e32 v45, v34
	v_mov_b32_e32 v46, v34
	v_mov_b32_e32 v47, v34
	v_mov_b32_e32 v48, v34
	v_mov_b32_e32 v49, v34
	v_mov_b32_e32 v58, v34
	v_mov_b32_e32 v59, v34
	v_mov_b32_e32 v60, v34
	v_mov_b32_e32 v61, v34
	v_mov_b32_e32 v62, v34
	v_mov_b32_e32 v63, v34
	v_mov_b32_e32 v64, v34
	v_mov_b32_e32 v65, v34
	v_mov_b32_e32 v74, v34
	v_mov_b32_e32 v75, v34
	v_mov_b32_e32 v76, v34
	v_mov_b32_e32 v77, v34
	v_mov_b32_e32 v78, v34
	v_mov_b32_e32 v79, v34
	v_mov_b32_e32 v80, v34
	v_mov_b32_e32 v81, v34
	v_mov_b32_e32 v90, v34
	v_mov_b32_e32 v91, v34
	v_mov_b32_e32 v92, v34
	v_mov_b32_e32 v93, v34
	v_mov_b32_e32 v94, v34
	v_mov_b32_e32 v95, v34
	v_mov_b32_e32 v96, v34
	v_mov_b32_e32 v97, v34
	v_mov_b32_e32 v98, v34
	v_mov_b32_e32 v99, v34
	v_mov_b32_e32 v100, v34
	v_mov_b32_e32 v101, v34
	v_mov_b32_e32 v102, v34
	v_mov_b32_e32 v103, v34
	v_mov_b32_e32 v104, v34
	v_mov_b32_e32 v105, v34
	v_mov_b32_e32 v114, v34
	v_mov_b32_e32 v115, v34
	v_mov_b32_e32 v116, v34
	v_mov_b32_e32 v117, v34
	v_mov_b32_e32 v118, v34
	v_mov_b32_e32 v119, v34
	v_mov_b32_e32 v120, v34
	v_mov_b32_e32 v121, v34
	v_mov_b32_e32 v130, v34
	v_mov_b32_e32 v131, v34
	v_mov_b32_e32 v132, v34
	v_mov_b32_e32 v133, v34
	v_mov_b32_e32 v134, v34
	v_mov_b32_e32 v135, v34
	v_mov_b32_e32 v136, v34
	v_mov_b32_e32 v137, v34
	v_mov_b32_e32 v150, v34
	v_mov_b32_e32 v151, v34
	v_mov_b32_e32 v152, v34
	v_mov_b32_e32 v153, v34
	v_mov_b32_e32 v154, v34
	v_mov_b32_e32 v155, v34
	v_mov_b32_e32 v156, v34
	v_mov_b32_e32 v157, v34
	v_mov_b32_e32 v106, v34
	v_mov_b32_e32 v107, v34
	v_mov_b32_e32 v108, v34
	v_mov_b32_e32 v109, v34
	v_mov_b32_e32 v110, v34
	v_mov_b32_e32 v111, v34
	v_mov_b32_e32 v112, v34
	v_mov_b32_e32 v113, v34
	v_mov_b32_e32 v122, v34
	v_mov_b32_e32 v123, v34
	v_mov_b32_e32 v124, v34
	v_mov_b32_e32 v125, v34
	v_mov_b32_e32 v126, v34
	v_mov_b32_e32 v127, v34
	v_mov_b32_e32 v128, v34
	v_mov_b32_e32 v129, v34
	v_mov_b32_e32 v138, v34
	v_mov_b32_e32 v139, v34
	v_mov_b32_e32 v140, v34
	v_mov_b32_e32 v141, v34
	v_mov_b32_e32 v142, v34
	v_mov_b32_e32 v143, v34
	v_mov_b32_e32 v144, v34
	v_mov_b32_e32 v145, v34
	v_mov_b32_e32 v158, v34
	v_mov_b32_e32 v159, v34
	v_mov_b32_e32 v160, v34
	v_mov_b32_e32 v161, v34
	v_mov_b32_e32 v146, v34
	v_mov_b32_e32 v147, v34
	v_mov_b32_e32 v148, v34
	v_mov_b32_e32 v149, v34
.LBB0_961:
	v_add_u32_e32 v2, 0x10000, v167
	v_add_u32_e32 v14, 0x14000, v167
	ds_read_b128 v[18:21], v2
	ds_read_b128 v[22:25], v2 offset:1024
	ds_read_b128 v[26:29], v2 offset:2048
	ds_read_b128 v[30:33], v2 offset:3072
	ds_read_b128 v[2:5], v14
	ds_read_b128 v[6:9], v14 offset:1024
	ds_read_b128 v[10:13], v14 offset:2048
	ds_read_b128 v[14:17], v14 offset:3072
	s_add_i32 m0, s41, 0xc000
	s_add_i32 s28, s41, 0xe000
	s_cmp_lg_u32 s19, s60
	s_cselect_b64 s[30:31], -1, 0
	v_lshl_add_u64 v[188:189], s[20:21], 0, v[194:195]
	v_lshl_add_u64 v[188:189], v[188:189], 0, s[26:27]
	v_mov_b32_e32 v169, v195
	ds_read_b128 v[180:183], v170
	ds_read_b128 v[184:187], v170 offset:1024
	ds_read_b128 v[216:219], v170 offset:2048
	ds_read_b128 v[220:223], v170 offset:3072
	ds_read_b128 v[224:227], v170 offset:4096
	ds_read_b128 v[228:231], v170 offset:5120
	ds_read_b128 v[196:199], v170 offset:6144
	ds_read_b128 v[200:203], v170 offset:7168
	global_load_lds_dwordx4 v[188:189], off
	v_lshl_add_u64 v[188:189], s[20:21], 0, v[168:169]
	v_lshl_add_u64 v[188:189], v[188:189], 0, s[26:27]
	s_mov_b32 m0, s28
	s_nop 0
	global_load_lds_dwordx4 v[188:189], off
	s_waitcnt vmcnt(8)
	s_waitcnt lgkmcnt(0)
	s_barrier
	s_setprio 1
	s_waitcnt lgkmcnt(0)
	v_mfma_f32_16x16x128_f8f6f4 v[146:149], v[18:25], v[180:187], v[146:149]
	v_mfma_f32_16x16x128_f8f6f4 v[158:161], v[26:33], v[180:187], v[158:161]
	v_mfma_f32_16x16x128_f8f6f4 v[142:145], v[18:25], v[216:223], v[142:145]
	v_mfma_f32_16x16x128_f8f6f4 v[138:141], v[26:33], v[216:223], v[138:141]
	v_mfma_f32_16x16x128_f8f6f4 v[126:129], v[18:25], v[224:231], v[126:129]
	v_mfma_f32_16x16x128_f8f6f4 v[122:125], v[26:33], v[224:231], v[122:125]
	v_mfma_f32_16x16x128_f8f6f4 v[110:113], v[18:25], v[196:203], v[110:113]
	v_mfma_f32_16x16x128_f8f6f4 v[106:109], v[26:33], v[196:203], v[106:109]
	s_setprio 0
	s_setprio 1
	v_mfma_f32_16x16x128_f8f6f4 v[154:157], v[2:9], v[180:187], v[154:157]
	v_mfma_f32_16x16x128_f8f6f4 v[150:153], v[10:17], v[180:187], v[150:153]
	v_mfma_f32_16x16x128_f8f6f4 v[134:137], v[2:9], v[216:223], v[134:137]
	v_mfma_f32_16x16x128_f8f6f4 v[130:133], v[10:17], v[216:223], v[130:133]
	v_mfma_f32_16x16x128_f8f6f4 v[118:121], v[2:9], v[224:231], v[118:121]
	v_mfma_f32_16x16x128_f8f6f4 v[114:117], v[10:17], v[224:231], v[114:117]
	v_mfma_f32_16x16x128_f8f6f4 v[102:105], v[2:9], v[196:203], v[102:105]
	v_mfma_f32_16x16x128_f8f6f4 v[98:101], v[10:17], v[196:203], v[98:101]
	s_setprio 0
	s_barrier
	s_and_b64 s[28:29], s[30:31], exec
	s_cselect_b32 s28, s60, 0
	s_or_b64 s[30:31], s[4:5], s[30:31]
	s_or_b64 s[66:67], s[30:31], s[22:23]
	s_and_b64 s[30:31], s[30:31], exec
	s_cselect_b32 s13, s13, s1
	s_cselect_b32 s12, s12, s0
	s_cselect_b32 s21, s21, s7
	s_cselect_b32 s20, s20, s6
	s_and_b64 vcc, exec, s[66:67]
	s_cbranch_vccnz .LBB0_963
	v_mov_b32_e32 v164, v0
	s_mov_b32 s28, 0
	v_ashrrev_i32_e32 v168, 31, v164
	v_lshrrev_b32_e32 v168, 26, v168
	v_lshlrev_b32_e32 v166, 4, v164
	v_add_u32_e32 v168, v164, v168
	v_bfe_i32 v164, v164, 27, 1
	v_lshrrev_b32_e32 v164, 22, v164
	v_add_u32_e32 v164, v166, v164
	v_and_b32_e32 v164, 0xfffffc00, v164
	v_sub_u32_e32 v164, v166, v164
	v_lshrrev_b32_e32 v169, 4, v164
	v_bitop3_b32 v169, v169, v164, 32 bitop3:0x6c
	v_ashrrev_i32_e32 v164, 31, v164
	v_lshrrev_b32_e32 v164, 26, v164
	v_add_u32_e32 v164, v169, v164
	v_and_b32_e32 v164, 0xc0, v164
	v_sub_u32_e32 v164, v169, v164
	v_lshrrev_b32_e32 v168, 1, v168
	v_ashrrev_i16_sdwa v164, v237, sext(v164) dst_sel:DWORD dst_unused:UNUSED_PAD src0_sel:DWORD src1_sel:BYTE_0
	v_and_b32_e32 v168, 32, v168
	v_bfe_i32 v164, v164, 0, 16
	v_add_lshl_u32 v168, v168, v164, 1
	v_add_u32_e32 v166, 0x2000, v166
	v_lshl_add_u32 v164, v172, 10, v168
	v_lshl_add_u32 v194, v173, 10, v168
	v_ashrrev_i32_e32 v168, 31, v166
	v_lshrrev_b32_e32 v168, 22, v168
	v_add_u32_e32 v168, v166, v168
	v_ashrrev_i32_e32 v168, 10, v168
	v_mul_i32_i24_e32 v169, 0x400, v168
	v_sub_u32_e32 v166, v166, v169
	v_lshrrev_b32_e32 v169, 4, v166
	v_bitop3_b32 v169, v169, v166, 32 bitop3:0x6c
	v_ashrrev_i32_e32 v166, 31, v166
	v_lshrrev_b32_e32 v166, 26, v166
	v_add_u32_e32 v166, v169, v166
	v_and_b32_e32 v166, 0xc0, v166
	v_sub_u32_e32 v166, v169, v166
	v_lshlrev_b32_e32 v168, 5, v168
	v_ashrrev_i16_sdwa v166, v237, sext(v166) dst_sel:DWORD dst_unused:UNUSED_PAD src0_sel:DWORD src1_sel:BYTE_0
	v_and_b32_e32 v168, 32, v168
	v_bfe_i32 v166, v166, 0, 16
	v_add_lshl_u32 v168, v168, v166, 1
	v_lshl_add_u32 v166, v174, 10, v168
	v_lshl_add_u32 v168, v175, 10, v168
	v_mov_b32_e32 v169, v195
	s_mov_b64 s[12:13], s[0:1]
	s_mov_b64 s[20:21], s[24:25]
